# speedup vs baseline: 1.0610x; 1.0610x over previous
_Z6scan_kPKDF16_S0_S0_S0_PKfPf:
	s_load_dwordx8 s[4:11], s[0:1], 0x0
	s_load_dwordx4 s[12:15], s[0:1], 0x20
	v_and_b32_e32 v1, 63, v0
	v_lshrrev_b32_e32 v2, 6, v0
	s_nop 1
	v_readfirstlane_b32 s16, v2
	s_lshr_b32 s17, s2, 7
	s_and_b32 s18, s2, 127
	s_lshl_b32 s18, s18, 2
	s_add_u32 s18, s18, s16
	s_lshl_b32 s19, s17, 9
	s_add_u32 s19, s19, s18
	s_mul_i32 s28, s16, 4608
	s_add_u32 s28, s28, 67584
	s_lshl_b32 s32, s16, 10
	s_add_u32 s33, s32, 0x1000
	s_add_u32 s34, s32, 0x2000
	s_add_u32 s35, s32, 0x3000
	s_mov_b32 s46, 0x200
	s_mov_b32 s47, 0
	s_mov_b32 s40, 0
	v_lshlrev_b32_e32 v2, 4, v1
	v_add_u32_e32 v3, 0x1000, v2
	v_add_u32_e32 v4, 0x2000, v2
	v_add_u32_e32 v5, 0x3000, v2
	v_lshlrev_b32_e32 v6, 2, v1
	v_lshlrev_b32_e32 v7, 1, v1
	v_and_b32_e32 v20, 7, v1
	v_lshlrev_b32_e32 v20, 1, v20
	v_add_u32_e32 v8, v2, v20
	v_add_u32_e32 v8, s28, v8
	v_and_b32_e32 v20, 3, v1
	v_bfe_u32 v21, v1, 3, 2
	v_lshl_add_u32 v20, v21, 2, v20
	v_lshrrev_b32_e32 v21, 5, v1
	v_bfe_u32 v22, v1, 2, 1
	v_bfe_u32 v23, v1, 4, 1
	v_cmp_eq_u32_e64 s[48:49], v21, v22
	v_cmp_eq_u32_e64 s[50:51], 0, v23
	s_nop 1
	s_and_b64 s[52:53], s[48:49], s[50:51]
	s_andn2_b64 s[54:55], s[48:49], s[50:51]
	v_mov_b32_e32 v24, 65536
	v_lshlrev_b32_e32 v25, 1, v20
	v_add_u32_e32 v25, s28, v25
	v_add_u32_e32 v26, 0x100, v25
	s_nop 1
	v_cndmask_b32_e64 v9, v24, v25, s[48:49]
	v_cndmask_b32_e64 v10, v24, v26, s[48:49]
	v_lshlrev_b32_e32 v25, 4, v20
	v_add_u32_e32 v25, s28, v25
	v_add_u32_e32 v25, 0x200, v25
	v_add_u32_e32 v26, 0x800, v25
	v_cndmask_b32_e64 v11, v24, v25, s[52:53]
	v_cndmask_b32_e64 v12, v24, v25, s[54:55]
	v_cndmask_b32_e64 v13, v24, v26, s[52:53]
	v_cndmask_b32_e64 v14, v24, v26, s[54:55]
	v_mov_b32_e32 v15, 1.0
	v_and_b32_e32 v89, 15, v1
	v_cmp_eq_u32_e64 s[42:43], 0, v89
	s_waitcnt lgkmcnt(0)
	s_lshl_b32 s30, s19, 13
	s_add_u32 s24, s4, s30
	s_addc_u32 s25, s5, 0
	s_add_u32 s26, s6, s30
	s_addc_u32 s27, s7, 0
	s_lshl_b32 s30, s17, 19
	s_add_u32 s30, s30, s32
	s_add_u32 s20, s8, s30
	s_addc_u32 s21, s9, 0
	s_add_u32 s22, s10, s30
	s_addc_u32 s23, s11, 0
	s_lshl_b32 s30, s18, 8
	s_add_u32 s12, s12, s30
	s_addc_u32 s13, s13, 0
	global_load_dword v90, v6, s[12:13]
	global_load_ushort v18, v7, s[26:27]
	global_load_ushort v19, v7, s[26:27] offset:128
	s_lshl_b32 s30, s19, 14
	s_add_u32 s14, s14, s30
	s_addc_u32 s15, s15, 0
	v_and_b32_e32 v30, 48, v1
	v_mov_b32_e32 v31, 0
	v_lshl_add_u64 v[16:17], s[14:15], 0, v[30:31]
	v_mov_b32_e32 v36, 0
	v_mov_b32_e32 v37, 0
	v_mov_b32_e32 v38, 0
	v_mov_b32_e32 v39, 0
	v_add_u32_e32 v29, 65536, v2
	ds_write_b128 v29, v[36:39]
	ds_write_b128 v29, v[36:39] offset:1024
	v_add_u32_e32 v29, s28, v2
	ds_write_b128 v29, v[36:39] offset:512
	ds_write_b128 v29, v[36:39] offset:1536
	ds_write_b128 v29, v[36:39] offset:2560
	ds_write_b128 v29, v[36:39] offset:3584
	s_mov_b32 m0, s32
	s_nop 0
	global_load_lds_dwordx4 v2, s[20:21]
	s_add_i32 m0, s32, 32768
	s_nop 0
	global_load_lds_dwordx4 v2, s[22:23]
	s_mov_b32 m0, s33
	s_nop 0
	global_load_lds_dwordx4 v3, s[20:21]
	s_add_i32 m0, s33, 32768
	s_nop 0
	global_load_lds_dwordx4 v3, s[22:23]
	s_mov_b32 m0, s34
	s_nop 0
	global_load_lds_dwordx4 v4, s[20:21]
	s_add_i32 m0, s34, 32768
	s_nop 0
	global_load_lds_dwordx4 v4, s[22:23]
	s_mov_b32 m0, s35
	s_nop 0
	global_load_lds_dwordx4 v5, s[20:21]
	s_add_i32 m0, s35, 32768
	s_nop 0
	global_load_lds_dwordx4 v5, s[22:23]
	s_mov_b32 m0, s28
	s_nop 0
	global_load_lds_dword v6, s[24:25]
	s_add_u32 s20, s20, 0x4000
	s_addc_u32 s21, s21, 0
	s_add_u32 s22, s22, 0x4000
	s_addc_u32 s23, s23, 0
	s_add_u32 s24, s24, 0x100
	s_addc_u32 s25, s25, 0
	s_add_i32 m0, s32, 0x4000
	s_nop 0
	global_load_lds_dwordx4 v2, s[20:21]
	s_add_i32 m0, s32, 49152
	s_nop 0
	global_load_lds_dwordx4 v2, s[22:23]
	s_add_i32 m0, s33, 0x4000
	s_nop 0
	global_load_lds_dwordx4 v3, s[20:21]
	s_add_i32 m0, s33, 49152
	s_nop 0
	global_load_lds_dwordx4 v3, s[22:23]
	s_add_i32 m0, s34, 0x4000
	s_nop 0
	global_load_lds_dwordx4 v4, s[20:21]
	s_add_i32 m0, s34, 49152
	s_nop 0
	global_load_lds_dwordx4 v4, s[22:23]
	s_add_i32 m0, s35, 0x4000
	s_nop 0
	global_load_lds_dwordx4 v5, s[20:21]
	s_add_i32 m0, s35, 49152
	s_nop 0
	global_load_lds_dwordx4 v5, s[22:23]
	s_add_i32 m0, s28, 0x100
	s_nop 0
	global_load_lds_dword v6, s[24:25]
	s_add_u32 s20, s20, 0x4000
	s_addc_u32 s21, s21, 0
	s_add_u32 s22, s22, 0x4000
	s_addc_u32 s23, s23, 0
	s_add_u32 s24, s24, 0x100
	s_addc_u32 s25, s25, 0
	s_mov_b32 s3, 0x3fb8aa3b
	s_waitcnt vmcnt(20)
	v_mul_f32_e32 v91, 0x3fb8aa3b, v90
	v_fma_f32 v92, v90, s3, -v91
	v_rndne_f32_e32 v93, v91
	v_fmamk_f32 v92, v90, 0x32a5705f, v92
	v_sub_f32_e32 v91, v91, v93
	v_add_f32_e32 v91, v91, v92
	v_exp_f32_e32 v91, v91
	v_cvt_i32_f32_e32 v92, v93
	s_mov_b32 s3, 0xc2ce8ed0
	v_cmp_ngt_f32_e32 vcc, s3, v90
	s_mov_b32 s3, 0x42b17218
	v_ldexp_f32 v91, v91, v92
	v_cndmask_b32_e32 v91, 0, v91, vcc
	v_mov_b32_e32 v92, 0x7f800000
	v_cmp_nlt_f32_e32 vcc, s3, v90
	s_mov_b32 s3, 0xbfb8aa3b
	s_nop 1
	v_cndmask_b32_e32 v90, v92, v91, vcc
	v_mov_b32_e32 v93, 0
	s_nop 0
	v_fma_mixlo_f16 v93, v90, s3, 0
	v_and_b32_e32 v28, 0xffff, v93
	v_mov_b32_e32 v29, 0
	v_mov_b32_e32 v30, 0
	v_mov_b32_e32 v31, 0
	v_mov_b32_e32 v32, 0
	v_mov_b32_e32 v33, 0
	v_mov_b32_e32 v34, 0
	v_mov_b32_e32 v35, 0
	v_mov_b32_e32 v94, 0x1c00
	v_mov_b32_e32 v95, 0x1c000000
	v_cmp_eq_u32_e32 vcc, 0, v89
	s_nop 1
	v_cndmask_b32_e32 v20, 0, v94, vcc
	v_cmp_eq_u32_e32 vcc, 1, v89
	s_nop 1
	v_cndmask_b32_e32 v20, v20, v95, vcc
	v_cmp_eq_u32_e32 vcc, 2, v89
	s_nop 1
	v_cndmask_b32_e32 v21, 0, v94, vcc
	v_cmp_eq_u32_e32 vcc, 3, v89
	s_nop 1
	v_cndmask_b32_e32 v21, v21, v95, vcc
	v_cmp_eq_u32_e32 vcc, 4, v89
	s_nop 1
	v_cndmask_b32_e32 v22, 0, v94, vcc
	v_cmp_eq_u32_e32 vcc, 5, v89
	s_nop 1
	v_cndmask_b32_e32 v22, v22, v95, vcc
	v_cmp_eq_u32_e32 vcc, 6, v89
	s_nop 1
	v_cndmask_b32_e32 v23, 0, v94, vcc
	v_cmp_eq_u32_e32 vcc, 7, v89
	s_nop 1
	v_cndmask_b32_e32 v23, v23, v95, vcc
	v_cmp_eq_u32_e32 vcc, 8, v89
	s_nop 1
	v_cndmask_b32_e32 v24, 0, v94, vcc
	v_cmp_eq_u32_e32 vcc, 9, v89
	s_nop 1
	v_cndmask_b32_e32 v24, v24, v95, vcc
	v_cmp_eq_u32_e32 vcc, 10, v89
	s_nop 1
	v_cndmask_b32_e32 v25, 0, v94, vcc
	v_cmp_eq_u32_e32 vcc, 11, v89
	s_nop 1
	v_cndmask_b32_e32 v25, v25, v95, vcc
	v_cmp_eq_u32_e32 vcc, 12, v89
	s_nop 1
	v_cndmask_b32_e32 v26, 0, v94, vcc
	v_cmp_eq_u32_e32 vcc, 13, v89
	s_nop 1
	v_cndmask_b32_e32 v26, v26, v95, vcc
	v_cmp_eq_u32_e32 vcc, 14, v89
	s_nop 1
	v_cndmask_b32_e32 v27, 0, v94, vcc
	v_cmp_eq_u32_e32 vcc, 15, v89
	s_nop 1
	v_cndmask_b32_e32 v27, v27, v95, vcc
	v_mov_b32_e32 v159, 0
	v_mov_b32_e32 v68, 0
	v_mov_b32_e32 v69, 0
	v_mov_b32_e32 v70, 0
	v_mov_b32_e32 v71, 0
	v_mov_b32_e32 v72, 0
	v_mov_b32_e32 v73, 0
	v_mov_b32_e32 v74, 0
	v_mov_b32_e32 v75, 0
	v_mov_b32_e32 v76, 0
	v_mov_b32_e32 v77, 0
	v_mov_b32_e32 v78, 0
	v_mov_b32_e32 v79, 0
	v_mov_b32_e32 v80, 0
	v_mov_b32_e32 v81, 0
	v_mov_b32_e32 v82, 0
	v_mov_b32_e32 v83, 0
	s_waitcnt vmcnt(18)
	ds_write_b16 v8, v18 offset:512
	ds_write_b16 v8, v19 offset:1536
	s_add_u32 s26, s26, 0x100
	s_addc_u32 s27, s27, 0
	global_load_ushort v18, v7, s[26:27]
	global_load_ushort v19, v7, s[26:27] offset:128
	s_add_u32 s26, s26, 0x100
	s_addc_u32 s27, s27, 0
	s_waitcnt vmcnt(0)
	s_waitcnt lgkmcnt(0)
	s_barrier
	ds_read_b128 v[52:55], v2 offset:32768
	ds_read_b128 v[56:59], v2 offset:33792
	ds_read_u16 v32, v9 offset:0
	ds_read_b128 v[36:39], v11 offset:0
	ds_read_b128 v[40:43], v12 offset:0
	ds_read_b128 v[44:47], v2 offset:0
	ds_read_b128 v[48:51], v2 offset:1024
	s_waitcnt lgkmcnt(0)
	v_mfma_f32_32x32x16_f16 v[96:111], v[32:35], v[28:31], 0
	v_mfma_f32_32x32x16_f16 v[128:143], v[36:39], v[44:47], 0
	v_mfma_f32_32x32x16_f16 v[128:143], v[40:43], v[48:51], v[128:143]
	ds_read_u16 v32, v9 offset:32
	ds_read_b128 v[36:39], v11 offset:256
	ds_read_b128 v[40:43], v12 offset:256
	ds_read_b128 v[44:47], v2 offset:2048
	ds_read_b128 v[48:51], v2 offset:3072
	s_nop 15
	s_nop 15
.Lscan_loop:
	ds_read_b128 v[60:63], v2 offset:34816
	ds_read_b128 v[64:67], v2 offset:35840
	v_mfma_f32_16x16x32_f16 v[80:83], v[72:75], v[24:27], v[80:83]
	v_exp_f32_e32 v96, v96
	v_exp_f32_e32 v97, v97
	v_exp_f32_e32 v98, v98
	v_exp_f32_e32 v99, v99
	s_waitcnt lgkmcnt(2)
	v_mfma_f32_32x32x16_f16 v[112:127], v[32:35], v[28:31], 0
	v_fmac_f32_e32 v128, v96, v159
	v_exp_f32_e32 v100, v100
	v_fmac_f32_e32 v129, v97, v128
	v_exp_f32_e32 v101, v101
	v_fmac_f32_e32 v130, v98, v129
	v_cvt_pkrtz_f16_f32 v68, v128, v129
	v_exp_f32_e32 v102, v102
	v_fmac_f32_e32 v131, v99, v130
	v_pk_mul_f16 v68, v52, v68
	v_exp_f32_e32 v103, v103
	v_mfma_f32_32x32x16_f16 v[144:159], v[36:39], v[44:47], 0
	v_fmac_f32_e32 v132, v100, v131
	v_cvt_pkrtz_f16_f32 v69, v130, v131
	v_exp_f32_e32 v104, v104
	v_fmac_f32_e32 v133, v101, v132
	v_pk_mul_f16 v69, v53, v69
	v_exp_f32_e32 v105, v105
	v_fmac_f32_e32 v134, v102, v133
	v_cvt_pkrtz_f16_f32 v70, v132, v133
	v_exp_f32_e32 v106, v106
	v_fmac_f32_e32 v135, v103, v134
	v_pk_mul_f16 v70, v54, v70
	v_exp_f32_e32 v107, v107
	v_mfma_f32_32x32x16_f16 v[144:159], v[40:43], v[48:51], v[144:159]
	v_cvt_pkrtz_f16_f32 v71, v134, v135
	v_fmac_f32_e32 v136, v104, v135
	ds_read_u16 v32, v9 offset:64
	ds_read_b128 v[36:39], v11 offset:512
	ds_read_b128 v[40:43], v12 offset:512
	ds_read_b128 v[44:47], v2 offset:4096
	ds_read_b128 v[48:51], v2 offset:5120
	v_pk_mul_f16 v71, v55, v71
	v_exp_f32_e32 v108, v108
	v_fmac_f32_e32 v137, v105, v136
	v_mfma_f32_16x16x32_f16 v[76:79], v[68:71], v[20:23], 0
	v_cvt_pkrtz_f16_f32 v72, v136, v137
	v_exp_f32_e32 v109, v109
	v_fmac_f32_e32 v138, v106, v137
	v_pk_mul_f16 v72, v56, v72
	v_add_f32_e32 v84, v80, v81
	v_fmac_f32_e32 v139, v107, v138
	v_cvt_pkrtz_f16_f32 v73, v138, v139
	v_exp_f32_e32 v110, v110
	v_fmac_f32_e32 v140, v108, v139
	v_pk_mul_f16 v73, v57, v73
	v_add_f32_e32 v85, v82, v83
	v_fmac_f32_e32 v141, v109, v140
	v_cvt_pkrtz_f16_f32 v74, v140, v141
	v_exp_f32_e32 v111, v111
	v_add_f32_e32 v84, v84, v85
	v_fmac_f32_e32 v142, v110, v141
	v_pk_mul_f16 v74, v58, v74
	v_fmac_f32_e32 v143, v111, v142
	v_mfma_f32_16x16x4_f32 a[28:31], v84, v15, 0
	v_cvt_pkrtz_f16_f32 v75, v142, v143
	v_pk_mul_f16 v75, v59, v75
	ds_read_b128 v[52:55], v2 offset:36864
	ds_read_b128 v[56:59], v2 offset:37888
	v_mfma_f32_16x16x32_f16 v[76:79], v[72:75], v[24:27], v[76:79]
	v_exp_f32_e32 v112, v112
	v_exp_f32_e32 v113, v113
	v_exp_f32_e32 v114, v114
	v_exp_f32_e32 v115, v115
	s_waitcnt lgkmcnt(2)
	v_mfma_f32_32x32x16_f16 v[96:111], v[32:35], v[28:31], 0
	v_fmac_f32_e32 v144, v112, v143
	v_exp_f32_e32 v116, v116
	v_fmac_f32_e32 v145, v113, v144
	v_exp_f32_e32 v117, v117
	v_fmac_f32_e32 v146, v114, v145
	v_cvt_pkrtz_f16_f32 v68, v144, v145
	v_exp_f32_e32 v118, v118
	v_fmac_f32_e32 v147, v115, v146
	v_pk_mul_f16 v68, v60, v68
	v_exp_f32_e32 v119, v119
	v_mfma_f32_32x32x16_f16 v[128:143], v[36:39], v[44:47], 0
	v_fmac_f32_e32 v148, v116, v147
	v_cvt_pkrtz_f16_f32 v69, v146, v147
	v_exp_f32_e32 v120, v120
	v_fmac_f32_e32 v149, v117, v148
	v_pk_mul_f16 v69, v61, v69
	v_exp_f32_e32 v121, v121
	v_fmac_f32_e32 v150, v118, v149
	v_cvt_pkrtz_f16_f32 v70, v148, v149
	v_exp_f32_e32 v122, v122
	v_fmac_f32_e32 v151, v119, v150
	v_pk_mul_f16 v70, v62, v70
	v_exp_f32_e32 v123, v123
	v_mfma_f32_32x32x16_f16 v[128:143], v[40:43], v[48:51], v[128:143]
	v_cvt_pkrtz_f16_f32 v71, v150, v151
	v_fmac_f32_e32 v152, v120, v151
	ds_read_u16 v32, v9 offset:96
	ds_read_b128 v[36:39], v11 offset:768
	ds_read_b128 v[40:43], v12 offset:768
	ds_read_b128 v[44:47], v2 offset:6144
	ds_read_b128 v[48:51], v2 offset:7168
	v_pk_mul_f16 v71, v63, v71
	v_exp_f32_e32 v124, v124
	v_fmac_f32_e32 v153, v121, v152
	v_mfma_f32_16x16x32_f16 v[80:83], v[68:71], v[20:23], 0
	v_cvt_pkrtz_f16_f32 v72, v152, v153
	v_exp_f32_e32 v125, v125
	v_fmac_f32_e32 v154, v122, v153
	v_pk_mul_f16 v72, v64, v72
	v_add_f32_e32 v84, v76, v77
	v_fmac_f32_e32 v155, v123, v154
	v_cvt_pkrtz_f16_f32 v73, v154, v155
	v_exp_f32_e32 v126, v126
	v_fmac_f32_e32 v156, v124, v155
	v_pk_mul_f16 v73, v65, v73
	v_add_f32_e32 v85, v78, v79
	v_fmac_f32_e32 v157, v125, v156
	v_cvt_pkrtz_f16_f32 v74, v156, v157
	v_exp_f32_e32 v127, v127
	v_add_f32_e32 v84, v84, v85
	v_fmac_f32_e32 v158, v126, v157
	v_pk_mul_f16 v74, v66, v74
	v_fmac_f32_e32 v159, v127, v158
	v_mfma_f32_16x16x4_f32 a[0:3], v84, v15, 0
	v_cvt_pkrtz_f16_f32 v75, v158, v159
	v_pk_mul_f16 v75, v67, v75
	ds_read_b128 v[60:63], v2 offset:38912
	ds_read_b128 v[64:67], v2 offset:39936
	v_mfma_f32_16x16x32_f16 v[80:83], v[72:75], v[24:27], v[80:83]
	v_exp_f32_e32 v96, v96
	v_exp_f32_e32 v97, v97
	v_exp_f32_e32 v98, v98
	v_exp_f32_e32 v99, v99
	s_waitcnt lgkmcnt(2)
	v_mfma_f32_32x32x16_f16 v[112:127], v[32:35], v[28:31], 0
	v_fmac_f32_e32 v128, v96, v159
	v_exp_f32_e32 v100, v100
	v_fmac_f32_e32 v129, v97, v128
	v_exp_f32_e32 v101, v101
	v_fmac_f32_e32 v130, v98, v129
	v_cvt_pkrtz_f16_f32 v68, v128, v129
	v_exp_f32_e32 v102, v102
	v_fmac_f32_e32 v131, v99, v130
	v_pk_mul_f16 v68, v52, v68
	v_exp_f32_e32 v103, v103
	v_mfma_f32_32x32x16_f16 v[144:159], v[36:39], v[44:47], 0
	v_fmac_f32_e32 v132, v100, v131
	v_cvt_pkrtz_f16_f32 v69, v130, v131
	v_exp_f32_e32 v104, v104
	v_fmac_f32_e32 v133, v101, v132
	v_pk_mul_f16 v69, v53, v69
	v_exp_f32_e32 v105, v105
	v_fmac_f32_e32 v134, v102, v133
	v_cvt_pkrtz_f16_f32 v70, v132, v133
	v_exp_f32_e32 v106, v106
	v_fmac_f32_e32 v135, v103, v134
	v_pk_mul_f16 v70, v54, v70
	v_exp_f32_e32 v107, v107
	v_mfma_f32_32x32x16_f16 v[144:159], v[40:43], v[48:51], v[144:159]
	v_cvt_pkrtz_f16_f32 v71, v134, v135
	v_fmac_f32_e32 v136, v104, v135
	ds_read_u16 v32, v9 offset:128
	ds_read_b128 v[36:39], v11 offset:1024
	ds_read_b128 v[40:43], v12 offset:1024
	ds_read_b128 v[44:47], v2 offset:8192
	ds_read_b128 v[48:51], v2 offset:9216
	v_pk_mul_f16 v71, v55, v71
	v_exp_f32_e32 v108, v108
	v_fmac_f32_e32 v137, v105, v136
	v_mfma_f32_16x16x32_f16 v[76:79], v[68:71], v[20:23], 0
	v_cvt_pkrtz_f16_f32 v72, v136, v137
	v_exp_f32_e32 v109, v109
	v_fmac_f32_e32 v138, v106, v137
	v_pk_mul_f16 v72, v56, v72
	v_add_f32_e32 v84, v80, v81
	v_fmac_f32_e32 v139, v107, v138
	v_cvt_pkrtz_f16_f32 v73, v138, v139
	v_exp_f32_e32 v110, v110
	v_fmac_f32_e32 v140, v108, v139
	v_pk_mul_f16 v73, v57, v73
	v_add_f32_e32 v85, v82, v83
	v_fmac_f32_e32 v141, v109, v140
	v_cvt_pkrtz_f16_f32 v74, v140, v141
	v_exp_f32_e32 v111, v111
	v_add_f32_e32 v84, v84, v85
	v_fmac_f32_e32 v142, v110, v141
	v_pk_mul_f16 v74, v58, v74
	v_fmac_f32_e32 v143, v111, v142
	v_mfma_f32_16x16x4_f32 a[4:7], v84, v15, 0
	v_cvt_pkrtz_f16_f32 v75, v142, v143
	v_pk_mul_f16 v75, v59, v75
	ds_read_b128 v[52:55], v2 offset:40960
	ds_read_b128 v[56:59], v2 offset:41984
	v_mfma_f32_16x16x32_f16 v[76:79], v[72:75], v[24:27], v[76:79]
	v_exp_f32_e32 v112, v112
	v_exp_f32_e32 v113, v113
	v_exp_f32_e32 v114, v114
	v_exp_f32_e32 v115, v115
	s_waitcnt lgkmcnt(2)
	v_mfma_f32_32x32x16_f16 v[96:111], v[32:35], v[28:31], 0
	v_fmac_f32_e32 v144, v112, v143
	v_exp_f32_e32 v116, v116
	v_fmac_f32_e32 v145, v113, v144
	v_exp_f32_e32 v117, v117
	v_fmac_f32_e32 v146, v114, v145
	v_cvt_pkrtz_f16_f32 v68, v144, v145
	v_exp_f32_e32 v118, v118
	v_fmac_f32_e32 v147, v115, v146
	v_pk_mul_f16 v68, v60, v68
	v_exp_f32_e32 v119, v119
	v_mfma_f32_32x32x16_f16 v[128:143], v[36:39], v[44:47], 0
	v_fmac_f32_e32 v148, v116, v147
	v_cvt_pkrtz_f16_f32 v69, v146, v147
	v_exp_f32_e32 v120, v120
	v_fmac_f32_e32 v149, v117, v148
	v_pk_mul_f16 v69, v61, v69
	v_exp_f32_e32 v121, v121
	v_fmac_f32_e32 v150, v118, v149
	v_cvt_pkrtz_f16_f32 v70, v148, v149
	v_exp_f32_e32 v122, v122
	v_fmac_f32_e32 v151, v119, v150
	v_pk_mul_f16 v70, v62, v70
	v_exp_f32_e32 v123, v123
	v_mfma_f32_32x32x16_f16 v[128:143], v[40:43], v[48:51], v[128:143]
	v_cvt_pkrtz_f16_f32 v71, v150, v151
	v_fmac_f32_e32 v152, v120, v151
	ds_read_u16 v32, v9 offset:160
	ds_read_b128 v[36:39], v11 offset:1280
	ds_read_b128 v[40:43], v12 offset:1280
	ds_read_b128 v[44:47], v2 offset:10240
	ds_read_b128 v[48:51], v2 offset:11264
	v_pk_mul_f16 v71, v63, v71
	v_exp_f32_e32 v124, v124
	v_fmac_f32_e32 v153, v121, v152
	v_mfma_f32_16x16x32_f16 v[80:83], v[68:71], v[20:23], 0
	v_cvt_pkrtz_f16_f32 v72, v152, v153
	v_exp_f32_e32 v125, v125
	v_fmac_f32_e32 v154, v122, v153
	v_pk_mul_f16 v72, v64, v72
	v_add_f32_e32 v84, v76, v77
	v_fmac_f32_e32 v155, v123, v154
	v_cvt_pkrtz_f16_f32 v73, v154, v155
	v_exp_f32_e32 v126, v126
	v_fmac_f32_e32 v156, v124, v155
	v_pk_mul_f16 v73, v65, v73
	v_add_f32_e32 v85, v78, v79
	v_fmac_f32_e32 v157, v125, v156
	v_cvt_pkrtz_f16_f32 v74, v156, v157
	v_exp_f32_e32 v127, v127
	v_add_f32_e32 v84, v84, v85
	v_fmac_f32_e32 v158, v126, v157
	v_pk_mul_f16 v74, v66, v74
	v_fmac_f32_e32 v159, v127, v158
	v_mfma_f32_16x16x4_f32 a[8:11], v84, v15, 0
	v_cvt_pkrtz_f16_f32 v75, v158, v159
	v_pk_mul_f16 v75, v67, v75
	ds_read_b128 v[60:63], v2 offset:43008
	ds_read_b128 v[64:67], v2 offset:44032
	v_mfma_f32_16x16x32_f16 v[80:83], v[72:75], v[24:27], v[80:83]
	v_exp_f32_e32 v96, v96
	v_exp_f32_e32 v97, v97
	v_exp_f32_e32 v98, v98
	v_exp_f32_e32 v99, v99
	s_waitcnt lgkmcnt(2)
	v_mfma_f32_32x32x16_f16 v[112:127], v[32:35], v[28:31], 0
	v_fmac_f32_e32 v128, v96, v159
	v_exp_f32_e32 v100, v100
	v_fmac_f32_e32 v129, v97, v128
	v_exp_f32_e32 v101, v101
	v_fmac_f32_e32 v130, v98, v129
	v_cvt_pkrtz_f16_f32 v68, v128, v129
	v_exp_f32_e32 v102, v102
	v_fmac_f32_e32 v131, v99, v130
	v_pk_mul_f16 v68, v52, v68
	v_exp_f32_e32 v103, v103
	v_mfma_f32_32x32x16_f16 v[144:159], v[36:39], v[44:47], 0
	v_fmac_f32_e32 v132, v100, v131
	v_cvt_pkrtz_f16_f32 v69, v130, v131
	v_exp_f32_e32 v104, v104
	v_fmac_f32_e32 v133, v101, v132
	v_pk_mul_f16 v69, v53, v69
	v_exp_f32_e32 v105, v105
	v_fmac_f32_e32 v134, v102, v133
	v_cvt_pkrtz_f16_f32 v70, v132, v133
	v_exp_f32_e32 v106, v106
	v_fmac_f32_e32 v135, v103, v134
	v_pk_mul_f16 v70, v54, v70
	v_exp_f32_e32 v107, v107
	v_mfma_f32_32x32x16_f16 v[144:159], v[40:43], v[48:51], v[144:159]
	v_cvt_pkrtz_f16_f32 v71, v134, v135
	v_fmac_f32_e32 v136, v104, v135
	ds_read_u16 v32, v9 offset:192
	ds_read_b128 v[36:39], v11 offset:1536
	ds_read_b128 v[40:43], v12 offset:1536
	ds_read_b128 v[44:47], v2 offset:12288
	ds_read_b128 v[48:51], v2 offset:13312
	v_pk_mul_f16 v71, v55, v71
	v_exp_f32_e32 v108, v108
	v_fmac_f32_e32 v137, v105, v136
	v_mfma_f32_16x16x32_f16 v[76:79], v[68:71], v[20:23], 0
	v_cvt_pkrtz_f16_f32 v72, v136, v137
	v_exp_f32_e32 v109, v109
	v_fmac_f32_e32 v138, v106, v137
	v_pk_mul_f16 v72, v56, v72
	v_add_f32_e32 v84, v80, v81
	v_fmac_f32_e32 v139, v107, v138
	v_cvt_pkrtz_f16_f32 v73, v138, v139
	v_exp_f32_e32 v110, v110
	v_fmac_f32_e32 v140, v108, v139
	v_pk_mul_f16 v73, v57, v73
	v_add_f32_e32 v85, v82, v83
	v_fmac_f32_e32 v141, v109, v140
	v_cvt_pkrtz_f16_f32 v74, v140, v141
	v_exp_f32_e32 v111, v111
	v_add_f32_e32 v84, v84, v85
	v_fmac_f32_e32 v142, v110, v141
	v_pk_mul_f16 v74, v58, v74
	v_fmac_f32_e32 v143, v111, v142
	v_mfma_f32_16x16x4_f32 a[12:15], v84, v15, 0
	v_cvt_pkrtz_f16_f32 v75, v142, v143
	v_pk_mul_f16 v75, v59, v75
	ds_read_b128 v[52:55], v2 offset:45056
	ds_read_b128 v[56:59], v2 offset:46080
	v_mfma_f32_16x16x32_f16 v[76:79], v[72:75], v[24:27], v[76:79]
	v_exp_f32_e32 v112, v112
	v_exp_f32_e32 v113, v113
	v_exp_f32_e32 v114, v114
	v_exp_f32_e32 v115, v115
	s_waitcnt lgkmcnt(2)
	v_mfma_f32_32x32x16_f16 v[96:111], v[32:35], v[28:31], 0
	v_fmac_f32_e32 v144, v112, v143
	v_exp_f32_e32 v116, v116
	v_fmac_f32_e32 v145, v113, v144
	v_exp_f32_e32 v117, v117
	v_fmac_f32_e32 v146, v114, v145
	v_cvt_pkrtz_f16_f32 v68, v144, v145
	v_exp_f32_e32 v118, v118
	v_fmac_f32_e32 v147, v115, v146
	v_pk_mul_f16 v68, v60, v68
	v_exp_f32_e32 v119, v119
	v_mfma_f32_32x32x16_f16 v[128:143], v[36:39], v[44:47], 0
	v_fmac_f32_e32 v148, v116, v147
	v_cvt_pkrtz_f16_f32 v69, v146, v147
	v_exp_f32_e32 v120, v120
	v_fmac_f32_e32 v149, v117, v148
	v_pk_mul_f16 v69, v61, v69
	v_exp_f32_e32 v121, v121
	v_fmac_f32_e32 v150, v118, v149
	v_cvt_pkrtz_f16_f32 v70, v148, v149
	v_exp_f32_e32 v122, v122
	v_fmac_f32_e32 v151, v119, v150
	v_pk_mul_f16 v70, v62, v70
	v_exp_f32_e32 v123, v123
	v_mfma_f32_32x32x16_f16 v[128:143], v[40:43], v[48:51], v[128:143]
	v_cvt_pkrtz_f16_f32 v71, v150, v151
	v_fmac_f32_e32 v152, v120, v151
	ds_read_u16 v32, v9 offset:224
	ds_read_b128 v[36:39], v11 offset:1792
	ds_read_b128 v[40:43], v12 offset:1792
	ds_read_b128 v[44:47], v2 offset:14336
	ds_read_b128 v[48:51], v2 offset:15360
	v_pk_mul_f16 v71, v63, v71
	v_exp_f32_e32 v124, v124
	v_fmac_f32_e32 v153, v121, v152
	v_mfma_f32_16x16x32_f16 v[80:83], v[68:71], v[20:23], 0
	v_cvt_pkrtz_f16_f32 v72, v152, v153
	v_exp_f32_e32 v125, v125
	v_fmac_f32_e32 v154, v122, v153
	v_pk_mul_f16 v72, v64, v72
	v_add_f32_e32 v84, v76, v77
	v_fmac_f32_e32 v155, v123, v154
	v_cvt_pkrtz_f16_f32 v73, v154, v155
	v_exp_f32_e32 v126, v126
	v_fmac_f32_e32 v156, v124, v155
	v_pk_mul_f16 v73, v65, v73
	v_add_f32_e32 v85, v78, v79
	v_fmac_f32_e32 v157, v125, v156
	v_cvt_pkrtz_f16_f32 v74, v156, v157
	v_exp_f32_e32 v127, v127
	v_add_f32_e32 v84, v84, v85
	v_fmac_f32_e32 v158, v126, v157
	v_pk_mul_f16 v74, v66, v74
	v_fmac_f32_e32 v159, v127, v158
	v_mfma_f32_16x16x4_f32 a[16:19], v84, v15, 0
	v_cvt_pkrtz_f16_f32 v75, v158, v159
	v_pk_mul_f16 v75, v67, v75
	ds_read_b128 v[60:63], v2 offset:47104
	ds_read_b128 v[64:67], v2 offset:48128
	v_mfma_f32_16x16x32_f16 v[80:83], v[72:75], v[24:27], v[80:83]
	s_waitcnt vmcnt(0)
	ds_write_b16 v8, v18 offset:2560
	ds_write_b16 v8, v19 offset:3584
	s_waitcnt lgkmcnt(0)
	s_barrier
	s_cmp_ge_u32 s40, 15
	s_cbranch_scc1 .Lscan_nodma0
	s_mov_b32 m0, s32
	s_nop 0
	global_load_lds_dwordx4 v2, s[20:21]
	s_add_i32 m0, s32, 32768
	s_nop 0
	global_load_lds_dwordx4 v2, s[22:23]
	s_mov_b32 m0, s33
	s_nop 0
	global_load_lds_dwordx4 v3, s[20:21]
	s_add_i32 m0, s33, 32768
	s_nop 0
	global_load_lds_dwordx4 v3, s[22:23]
	s_mov_b32 m0, s34
	s_nop 0
	global_load_lds_dwordx4 v4, s[20:21]
	s_add_i32 m0, s34, 32768
	s_nop 0
	global_load_lds_dwordx4 v4, s[22:23]
	s_mov_b32 m0, s35
	s_nop 0
	global_load_lds_dwordx4 v5, s[20:21]
	s_add_i32 m0, s35, 32768
	s_nop 0
	global_load_lds_dwordx4 v5, s[22:23]
	s_mov_b32 m0, s28
	s_nop 0
	global_load_lds_dword v6, s[24:25]
	global_load_ushort v18, v7, s[26:27]
	global_load_ushort v19, v7, s[26:27] offset:128
	s_add_u32 s20, s20, 0x4000
	s_addc_u32 s21, s21, 0
	s_add_u32 s22, s22, 0x4000
	s_addc_u32 s23, s23, 0
	s_add_u32 s24, s24, 0x100
	s_addc_u32 s25, s25, 0
	s_add_u32 s26, s26, 0x100
	s_addc_u32 s27, s27, 0
.Lscan_nodma0:
	s_and_saveexec_b64 s[44:45], s[42:43]
	s_cmp_eq_u32 s40, 0
	s_cbranch_scc1 .Lscan_nocarry
	global_store_dwordx4 v[16:17], a[20:23], off offset:-192
	global_store_dwordx4 v[16:17], a[24:27], off offset:-128
	global_store_dwordx4 v[16:17], a[28:31], off offset:-64
.Lscan_nocarry:
	global_store_dwordx4 v[16:17], a[0:3], off
	global_store_dwordx4 v[16:17], a[4:7], off offset:64
	global_store_dwordx4 v[16:17], a[8:11], off offset:128
	global_store_dwordx4 v[16:17], a[12:15], off offset:192
	global_store_dwordx4 v[16:17], a[16:19], off offset:256
	s_mov_b64 exec, s[44:45]
	v_lshl_add_u64 v[16:17], v[16:17], 0, s[46:47]
	v_exp_f32_e32 v96, v96
	v_exp_f32_e32 v97, v97
	v_exp_f32_e32 v98, v98
	v_exp_f32_e32 v99, v99
	s_waitcnt lgkmcnt(2)
	v_mfma_f32_32x32x16_f16 v[112:127], v[32:35], v[28:31], 0
	v_fmac_f32_e32 v128, v96, v159
	v_exp_f32_e32 v100, v100
	v_fmac_f32_e32 v129, v97, v128
	v_exp_f32_e32 v101, v101
	v_fmac_f32_e32 v130, v98, v129
	v_cvt_pkrtz_f16_f32 v68, v128, v129
	v_exp_f32_e32 v102, v102
	v_fmac_f32_e32 v131, v99, v130
	v_pk_mul_f16 v68, v52, v68
	v_exp_f32_e32 v103, v103
	v_mfma_f32_32x32x16_f16 v[144:159], v[36:39], v[44:47], 0
	v_fmac_f32_e32 v132, v100, v131
	v_cvt_pkrtz_f16_f32 v69, v130, v131
	v_exp_f32_e32 v104, v104
	v_fmac_f32_e32 v133, v101, v132
	v_pk_mul_f16 v69, v53, v69
	v_exp_f32_e32 v105, v105
	v_fmac_f32_e32 v134, v102, v133
	v_cvt_pkrtz_f16_f32 v70, v132, v133
	v_exp_f32_e32 v106, v106
	v_fmac_f32_e32 v135, v103, v134
	v_pk_mul_f16 v70, v54, v70
	v_exp_f32_e32 v107, v107
	v_mfma_f32_32x32x16_f16 v[144:159], v[40:43], v[48:51], v[144:159]
	v_cvt_pkrtz_f16_f32 v71, v134, v135
	v_fmac_f32_e32 v136, v104, v135
	ds_read_u16 v32, v10 offset:0
	ds_read_b128 v[36:39], v13 offset:0
	ds_read_b128 v[40:43], v14 offset:0
	ds_read_b128 v[44:47], v2 offset:16384
	ds_read_b128 v[48:51], v2 offset:17408
	v_pk_mul_f16 v71, v55, v71
	v_exp_f32_e32 v108, v108
	v_fmac_f32_e32 v137, v105, v136
	v_mfma_f32_16x16x32_f16 v[76:79], v[68:71], v[20:23], 0
	v_cvt_pkrtz_f16_f32 v72, v136, v137
	v_exp_f32_e32 v109, v109
	v_fmac_f32_e32 v138, v106, v137
	v_pk_mul_f16 v72, v56, v72
	v_add_f32_e32 v84, v80, v81
	v_fmac_f32_e32 v139, v107, v138
	v_cvt_pkrtz_f16_f32 v73, v138, v139
	v_exp_f32_e32 v110, v110
	v_fmac_f32_e32 v140, v108, v139
	v_pk_mul_f16 v73, v57, v73
	v_add_f32_e32 v85, v82, v83
	v_fmac_f32_e32 v141, v109, v140
	v_cvt_pkrtz_f16_f32 v74, v140, v141
	v_exp_f32_e32 v111, v111
	v_add_f32_e32 v84, v84, v85
	v_fmac_f32_e32 v142, v110, v141
	v_pk_mul_f16 v74, v58, v74
	v_fmac_f32_e32 v143, v111, v142
	v_mfma_f32_16x16x4_f32 a[20:23], v84, v15, 0
	v_cvt_pkrtz_f16_f32 v75, v142, v143
	v_pk_mul_f16 v75, v59, v75
	ds_read_b128 v[52:55], v2 offset:49152
	ds_read_b128 v[56:59], v2 offset:50176
	v_mfma_f32_16x16x32_f16 v[76:79], v[72:75], v[24:27], v[76:79]
	v_exp_f32_e32 v112, v112
	v_exp_f32_e32 v113, v113
	v_exp_f32_e32 v114, v114
	v_exp_f32_e32 v115, v115
	s_waitcnt lgkmcnt(2)
	v_mfma_f32_32x32x16_f16 v[96:111], v[32:35], v[28:31], 0
	v_fmac_f32_e32 v144, v112, v143
	v_exp_f32_e32 v116, v116
	v_fmac_f32_e32 v145, v113, v144
	v_exp_f32_e32 v117, v117
	v_fmac_f32_e32 v146, v114, v145
	v_cvt_pkrtz_f16_f32 v68, v144, v145
	v_exp_f32_e32 v118, v118
	v_fmac_f32_e32 v147, v115, v146
	v_pk_mul_f16 v68, v60, v68
	v_exp_f32_e32 v119, v119
	v_mfma_f32_32x32x16_f16 v[128:143], v[36:39], v[44:47], 0
	v_fmac_f32_e32 v148, v116, v147
	v_cvt_pkrtz_f16_f32 v69, v146, v147
	v_exp_f32_e32 v120, v120
	v_fmac_f32_e32 v149, v117, v148
	v_pk_mul_f16 v69, v61, v69
	v_exp_f32_e32 v121, v121
	v_fmac_f32_e32 v150, v118, v149
	v_cvt_pkrtz_f16_f32 v70, v148, v149
	v_exp_f32_e32 v122, v122
	v_fmac_f32_e32 v151, v119, v150
	v_pk_mul_f16 v70, v62, v70
	v_exp_f32_e32 v123, v123
	v_mfma_f32_32x32x16_f16 v[128:143], v[40:43], v[48:51], v[128:143]
	v_cvt_pkrtz_f16_f32 v71, v150, v151
	v_fmac_f32_e32 v152, v120, v151
	ds_read_u16 v32, v10 offset:32
	ds_read_b128 v[36:39], v13 offset:256
	ds_read_b128 v[40:43], v14 offset:256
	ds_read_b128 v[44:47], v2 offset:18432
	ds_read_b128 v[48:51], v2 offset:19456
	v_pk_mul_f16 v71, v63, v71
	v_exp_f32_e32 v124, v124
	v_fmac_f32_e32 v153, v121, v152
	v_mfma_f32_16x16x32_f16 v[80:83], v[68:71], v[20:23], 0
	v_cvt_pkrtz_f16_f32 v72, v152, v153
	v_exp_f32_e32 v125, v125
	v_fmac_f32_e32 v154, v122, v153
	v_pk_mul_f16 v72, v64, v72
	v_add_f32_e32 v84, v76, v77
	v_fmac_f32_e32 v155, v123, v154
	v_cvt_pkrtz_f16_f32 v73, v154, v155
	v_exp_f32_e32 v126, v126
	v_fmac_f32_e32 v156, v124, v155
	v_pk_mul_f16 v73, v65, v73
	v_add_f32_e32 v85, v78, v79
	v_fmac_f32_e32 v157, v125, v156
	v_cvt_pkrtz_f16_f32 v74, v156, v157
	v_exp_f32_e32 v127, v127
	v_add_f32_e32 v84, v84, v85
	v_fmac_f32_e32 v158, v126, v157
	v_pk_mul_f16 v74, v66, v74
	v_fmac_f32_e32 v159, v127, v158
	v_mfma_f32_16x16x4_f32 a[24:27], v84, v15, 0
	v_cvt_pkrtz_f16_f32 v75, v158, v159
	v_pk_mul_f16 v75, v67, v75
	ds_read_b128 v[60:63], v2 offset:51200
	ds_read_b128 v[64:67], v2 offset:52224
	v_mfma_f32_16x16x32_f16 v[80:83], v[72:75], v[24:27], v[80:83]
	v_exp_f32_e32 v96, v96
	v_exp_f32_e32 v97, v97
	v_exp_f32_e32 v98, v98
	v_exp_f32_e32 v99, v99
	s_waitcnt lgkmcnt(2)
	v_mfma_f32_32x32x16_f16 v[112:127], v[32:35], v[28:31], 0
	v_fmac_f32_e32 v128, v96, v159
	v_exp_f32_e32 v100, v100
	v_fmac_f32_e32 v129, v97, v128
	v_exp_f32_e32 v101, v101
	v_fmac_f32_e32 v130, v98, v129
	v_cvt_pkrtz_f16_f32 v68, v128, v129
	v_exp_f32_e32 v102, v102
	v_fmac_f32_e32 v131, v99, v130
	v_pk_mul_f16 v68, v52, v68
	v_exp_f32_e32 v103, v103
	v_mfma_f32_32x32x16_f16 v[144:159], v[36:39], v[44:47], 0
	v_fmac_f32_e32 v132, v100, v131
	v_cvt_pkrtz_f16_f32 v69, v130, v131
	v_exp_f32_e32 v104, v104
	v_fmac_f32_e32 v133, v101, v132
	v_pk_mul_f16 v69, v53, v69
	v_exp_f32_e32 v105, v105
	v_fmac_f32_e32 v134, v102, v133
	v_cvt_pkrtz_f16_f32 v70, v132, v133
	v_exp_f32_e32 v106, v106
	v_fmac_f32_e32 v135, v103, v134
	v_pk_mul_f16 v70, v54, v70
	v_exp_f32_e32 v107, v107
	v_mfma_f32_32x32x16_f16 v[144:159], v[40:43], v[48:51], v[144:159]
	v_cvt_pkrtz_f16_f32 v71, v134, v135
	v_fmac_f32_e32 v136, v104, v135
	ds_read_u16 v32, v10 offset:64
	ds_read_b128 v[36:39], v13 offset:512
	ds_read_b128 v[40:43], v14 offset:512
	ds_read_b128 v[44:47], v2 offset:20480
	ds_read_b128 v[48:51], v2 offset:21504
	v_pk_mul_f16 v71, v55, v71
	v_exp_f32_e32 v108, v108
	v_fmac_f32_e32 v137, v105, v136
	v_mfma_f32_16x16x32_f16 v[76:79], v[68:71], v[20:23], 0
	v_cvt_pkrtz_f16_f32 v72, v136, v137
	v_exp_f32_e32 v109, v109
	v_fmac_f32_e32 v138, v106, v137
	v_pk_mul_f16 v72, v56, v72
	v_add_f32_e32 v84, v80, v81
	v_fmac_f32_e32 v139, v107, v138
	v_cvt_pkrtz_f16_f32 v73, v138, v139
	v_exp_f32_e32 v110, v110
	v_fmac_f32_e32 v140, v108, v139
	v_pk_mul_f16 v73, v57, v73
	v_add_f32_e32 v85, v82, v83
	v_fmac_f32_e32 v141, v109, v140
	v_cvt_pkrtz_f16_f32 v74, v140, v141
	v_exp_f32_e32 v111, v111
	v_add_f32_e32 v84, v84, v85
	v_fmac_f32_e32 v142, v110, v141
	v_pk_mul_f16 v74, v58, v74
	v_fmac_f32_e32 v143, v111, v142
	v_mfma_f32_16x16x4_f32 a[28:31], v84, v15, 0
	v_cvt_pkrtz_f16_f32 v75, v142, v143
	v_pk_mul_f16 v75, v59, v75
	ds_read_b128 v[52:55], v2 offset:53248
	ds_read_b128 v[56:59], v2 offset:54272
	v_mfma_f32_16x16x32_f16 v[76:79], v[72:75], v[24:27], v[76:79]
	v_exp_f32_e32 v112, v112
	v_exp_f32_e32 v113, v113
	v_exp_f32_e32 v114, v114
	v_exp_f32_e32 v115, v115
	s_waitcnt lgkmcnt(2)
	v_mfma_f32_32x32x16_f16 v[96:111], v[32:35], v[28:31], 0
	v_fmac_f32_e32 v144, v112, v143
	v_exp_f32_e32 v116, v116
	v_fmac_f32_e32 v145, v113, v144
	v_exp_f32_e32 v117, v117
	v_fmac_f32_e32 v146, v114, v145
	v_cvt_pkrtz_f16_f32 v68, v144, v145
	v_exp_f32_e32 v118, v118
	v_fmac_f32_e32 v147, v115, v146
	v_pk_mul_f16 v68, v60, v68
	v_exp_f32_e32 v119, v119
	v_mfma_f32_32x32x16_f16 v[128:143], v[36:39], v[44:47], 0
	v_fmac_f32_e32 v148, v116, v147
	v_cvt_pkrtz_f16_f32 v69, v146, v147
	v_exp_f32_e32 v120, v120
	v_fmac_f32_e32 v149, v117, v148
	v_pk_mul_f16 v69, v61, v69
	v_exp_f32_e32 v121, v121
	v_fmac_f32_e32 v150, v118, v149
	v_cvt_pkrtz_f16_f32 v70, v148, v149
	v_exp_f32_e32 v122, v122
	v_fmac_f32_e32 v151, v119, v150
	v_pk_mul_f16 v70, v62, v70
	v_exp_f32_e32 v123, v123
	v_mfma_f32_32x32x16_f16 v[128:143], v[40:43], v[48:51], v[128:143]
	v_cvt_pkrtz_f16_f32 v71, v150, v151
	v_fmac_f32_e32 v152, v120, v151
	ds_read_u16 v32, v10 offset:96
	ds_read_b128 v[36:39], v13 offset:768
	ds_read_b128 v[40:43], v14 offset:768
	ds_read_b128 v[44:47], v2 offset:22528
	ds_read_b128 v[48:51], v2 offset:23552
	v_pk_mul_f16 v71, v63, v71
	v_exp_f32_e32 v124, v124
	v_fmac_f32_e32 v153, v121, v152
	v_mfma_f32_16x16x32_f16 v[80:83], v[68:71], v[20:23], 0
	v_cvt_pkrtz_f16_f32 v72, v152, v153
	v_exp_f32_e32 v125, v125
	v_fmac_f32_e32 v154, v122, v153
	v_pk_mul_f16 v72, v64, v72
	v_add_f32_e32 v84, v76, v77
	v_fmac_f32_e32 v155, v123, v154
	v_cvt_pkrtz_f16_f32 v73, v154, v155
	v_exp_f32_e32 v126, v126
	v_fmac_f32_e32 v156, v124, v155
	v_pk_mul_f16 v73, v65, v73
	v_add_f32_e32 v85, v78, v79
	v_fmac_f32_e32 v157, v125, v156
	v_cvt_pkrtz_f16_f32 v74, v156, v157
	v_exp_f32_e32 v127, v127
	v_add_f32_e32 v84, v84, v85
	v_fmac_f32_e32 v158, v126, v157
	v_pk_mul_f16 v74, v66, v74
	v_fmac_f32_e32 v159, v127, v158
	v_mfma_f32_16x16x4_f32 a[0:3], v84, v15, 0
	v_cvt_pkrtz_f16_f32 v75, v158, v159
	v_pk_mul_f16 v75, v67, v75
	ds_read_b128 v[60:63], v2 offset:55296
	ds_read_b128 v[64:67], v2 offset:56320
	v_mfma_f32_16x16x32_f16 v[80:83], v[72:75], v[24:27], v[80:83]
	v_exp_f32_e32 v96, v96
	v_exp_f32_e32 v97, v97
	v_exp_f32_e32 v98, v98
	v_exp_f32_e32 v99, v99
	s_waitcnt lgkmcnt(2)
	v_mfma_f32_32x32x16_f16 v[112:127], v[32:35], v[28:31], 0
	v_fmac_f32_e32 v128, v96, v159
	v_exp_f32_e32 v100, v100
	v_fmac_f32_e32 v129, v97, v128
	v_exp_f32_e32 v101, v101
	v_fmac_f32_e32 v130, v98, v129
	v_cvt_pkrtz_f16_f32 v68, v128, v129
	v_exp_f32_e32 v102, v102
	v_fmac_f32_e32 v131, v99, v130
	v_pk_mul_f16 v68, v52, v68
	v_exp_f32_e32 v103, v103
	v_mfma_f32_32x32x16_f16 v[144:159], v[36:39], v[44:47], 0
	v_fmac_f32_e32 v132, v100, v131
	v_cvt_pkrtz_f16_f32 v69, v130, v131
	v_exp_f32_e32 v104, v104
	v_fmac_f32_e32 v133, v101, v132
	v_pk_mul_f16 v69, v53, v69
	v_exp_f32_e32 v105, v105
	v_fmac_f32_e32 v134, v102, v133
	v_cvt_pkrtz_f16_f32 v70, v132, v133
	v_exp_f32_e32 v106, v106
	v_fmac_f32_e32 v135, v103, v134
	v_pk_mul_f16 v70, v54, v70
	v_exp_f32_e32 v107, v107
	v_mfma_f32_32x32x16_f16 v[144:159], v[40:43], v[48:51], v[144:159]
	v_cvt_pkrtz_f16_f32 v71, v134, v135
	v_fmac_f32_e32 v136, v104, v135
	ds_read_u16 v32, v10 offset:128
	ds_read_b128 v[36:39], v13 offset:1024
	ds_read_b128 v[40:43], v14 offset:1024
	ds_read_b128 v[44:47], v2 offset:24576
	ds_read_b128 v[48:51], v2 offset:25600
	v_pk_mul_f16 v71, v55, v71
	v_exp_f32_e32 v108, v108
	v_fmac_f32_e32 v137, v105, v136
	v_mfma_f32_16x16x32_f16 v[76:79], v[68:71], v[20:23], 0
	v_cvt_pkrtz_f16_f32 v72, v136, v137
	v_exp_f32_e32 v109, v109
	v_fmac_f32_e32 v138, v106, v137
	v_pk_mul_f16 v72, v56, v72
	v_add_f32_e32 v84, v80, v81
	v_fmac_f32_e32 v139, v107, v138
	v_cvt_pkrtz_f16_f32 v73, v138, v139
	v_exp_f32_e32 v110, v110
	v_fmac_f32_e32 v140, v108, v139
	v_pk_mul_f16 v73, v57, v73
	v_add_f32_e32 v85, v82, v83
	v_fmac_f32_e32 v141, v109, v140
	v_cvt_pkrtz_f16_f32 v74, v140, v141
	v_exp_f32_e32 v111, v111
	v_add_f32_e32 v84, v84, v85
	v_fmac_f32_e32 v142, v110, v141
	v_pk_mul_f16 v74, v58, v74
	v_fmac_f32_e32 v143, v111, v142
	v_mfma_f32_16x16x4_f32 a[4:7], v84, v15, 0
	v_cvt_pkrtz_f16_f32 v75, v142, v143
	v_pk_mul_f16 v75, v59, v75
	ds_read_b128 v[52:55], v2 offset:57344
	ds_read_b128 v[56:59], v2 offset:58368
	v_mfma_f32_16x16x32_f16 v[76:79], v[72:75], v[24:27], v[76:79]
	v_exp_f32_e32 v112, v112
	v_exp_f32_e32 v113, v113
	v_exp_f32_e32 v114, v114
	v_exp_f32_e32 v115, v115
	s_waitcnt lgkmcnt(2)
	v_mfma_f32_32x32x16_f16 v[96:111], v[32:35], v[28:31], 0
	v_fmac_f32_e32 v144, v112, v143
	v_exp_f32_e32 v116, v116
	v_fmac_f32_e32 v145, v113, v144
	v_exp_f32_e32 v117, v117
	v_fmac_f32_e32 v146, v114, v145
	v_cvt_pkrtz_f16_f32 v68, v144, v145
	v_exp_f32_e32 v118, v118
	v_fmac_f32_e32 v147, v115, v146
	v_pk_mul_f16 v68, v60, v68
	v_exp_f32_e32 v119, v119
	v_mfma_f32_32x32x16_f16 v[128:143], v[36:39], v[44:47], 0
	v_fmac_f32_e32 v148, v116, v147
	v_cvt_pkrtz_f16_f32 v69, v146, v147
	v_exp_f32_e32 v120, v120
	v_fmac_f32_e32 v149, v117, v148
	v_pk_mul_f16 v69, v61, v69
	v_exp_f32_e32 v121, v121
	v_fmac_f32_e32 v150, v118, v149
	v_cvt_pkrtz_f16_f32 v70, v148, v149
	v_exp_f32_e32 v122, v122
	v_fmac_f32_e32 v151, v119, v150
	v_pk_mul_f16 v70, v62, v70
	v_exp_f32_e32 v123, v123
	v_mfma_f32_32x32x16_f16 v[128:143], v[40:43], v[48:51], v[128:143]
	v_cvt_pkrtz_f16_f32 v71, v150, v151
	v_fmac_f32_e32 v152, v120, v151
	ds_read_u16 v32, v10 offset:160
	ds_read_b128 v[36:39], v13 offset:1280
	ds_read_b128 v[40:43], v14 offset:1280
	ds_read_b128 v[44:47], v2 offset:26624
	ds_read_b128 v[48:51], v2 offset:27648
	v_pk_mul_f16 v71, v63, v71
	v_exp_f32_e32 v124, v124
	v_fmac_f32_e32 v153, v121, v152
	v_mfma_f32_16x16x32_f16 v[80:83], v[68:71], v[20:23], 0
	v_cvt_pkrtz_f16_f32 v72, v152, v153
	v_exp_f32_e32 v125, v125
	v_fmac_f32_e32 v154, v122, v153
	v_pk_mul_f16 v72, v64, v72
	v_add_f32_e32 v84, v76, v77
	v_fmac_f32_e32 v155, v123, v154
	v_cvt_pkrtz_f16_f32 v73, v154, v155
	v_exp_f32_e32 v126, v126
	v_fmac_f32_e32 v156, v124, v155
	v_pk_mul_f16 v73, v65, v73
	v_add_f32_e32 v85, v78, v79
	v_fmac_f32_e32 v157, v125, v156
	v_cvt_pkrtz_f16_f32 v74, v156, v157
	v_exp_f32_e32 v127, v127
	v_add_f32_e32 v84, v84, v85
	v_fmac_f32_e32 v158, v126, v157
	v_pk_mul_f16 v74, v66, v74
	v_fmac_f32_e32 v159, v127, v158
	v_mfma_f32_16x16x4_f32 a[8:11], v84, v15, 0
	v_cvt_pkrtz_f16_f32 v75, v158, v159
	v_pk_mul_f16 v75, v67, v75
	ds_read_b128 v[60:63], v2 offset:59392
	ds_read_b128 v[64:67], v2 offset:60416
	v_mfma_f32_16x16x32_f16 v[80:83], v[72:75], v[24:27], v[80:83]
	v_exp_f32_e32 v96, v96
	v_exp_f32_e32 v97, v97
	v_exp_f32_e32 v98, v98
	v_exp_f32_e32 v99, v99
	s_waitcnt lgkmcnt(2)
	v_mfma_f32_32x32x16_f16 v[112:127], v[32:35], v[28:31], 0
	v_fmac_f32_e32 v128, v96, v159
	v_exp_f32_e32 v100, v100
	v_fmac_f32_e32 v129, v97, v128
	v_exp_f32_e32 v101, v101
	v_fmac_f32_e32 v130, v98, v129
	v_cvt_pkrtz_f16_f32 v68, v128, v129
	v_exp_f32_e32 v102, v102
	v_fmac_f32_e32 v131, v99, v130
	v_pk_mul_f16 v68, v52, v68
	v_exp_f32_e32 v103, v103
	v_mfma_f32_32x32x16_f16 v[144:159], v[36:39], v[44:47], 0
	v_fmac_f32_e32 v132, v100, v131
	v_cvt_pkrtz_f16_f32 v69, v130, v131
	v_exp_f32_e32 v104, v104
	v_fmac_f32_e32 v133, v101, v132
	v_pk_mul_f16 v69, v53, v69
	v_exp_f32_e32 v105, v105
	v_fmac_f32_e32 v134, v102, v133
	v_cvt_pkrtz_f16_f32 v70, v132, v133
	v_exp_f32_e32 v106, v106
	v_fmac_f32_e32 v135, v103, v134
	v_pk_mul_f16 v70, v54, v70
	v_exp_f32_e32 v107, v107
	v_mfma_f32_32x32x16_f16 v[144:159], v[40:43], v[48:51], v[144:159]
	v_cvt_pkrtz_f16_f32 v71, v134, v135
	v_fmac_f32_e32 v136, v104, v135
	ds_read_u16 v32, v10 offset:192
	ds_read_b128 v[36:39], v13 offset:1536
	ds_read_b128 v[40:43], v14 offset:1536
	ds_read_b128 v[44:47], v2 offset:28672
	ds_read_b128 v[48:51], v2 offset:29696
	v_pk_mul_f16 v71, v55, v71
	v_exp_f32_e32 v108, v108
	v_fmac_f32_e32 v137, v105, v136
	v_mfma_f32_16x16x32_f16 v[76:79], v[68:71], v[20:23], 0
	v_cvt_pkrtz_f16_f32 v72, v136, v137
	v_exp_f32_e32 v109, v109
	v_fmac_f32_e32 v138, v106, v137
	v_pk_mul_f16 v72, v56, v72
	v_add_f32_e32 v84, v80, v81
	v_fmac_f32_e32 v139, v107, v138
	v_cvt_pkrtz_f16_f32 v73, v138, v139
	v_exp_f32_e32 v110, v110
	v_fmac_f32_e32 v140, v108, v139
	v_pk_mul_f16 v73, v57, v73
	v_add_f32_e32 v85, v82, v83
	v_fmac_f32_e32 v141, v109, v140
	v_cvt_pkrtz_f16_f32 v74, v140, v141
	v_exp_f32_e32 v111, v111
	v_add_f32_e32 v84, v84, v85
	v_fmac_f32_e32 v142, v110, v141
	v_pk_mul_f16 v74, v58, v74
	v_fmac_f32_e32 v143, v111, v142
	v_mfma_f32_16x16x4_f32 a[12:15], v84, v15, 0
	v_cvt_pkrtz_f16_f32 v75, v142, v143
	v_pk_mul_f16 v75, v59, v75
	ds_read_b128 v[52:55], v2 offset:61440
	ds_read_b128 v[56:59], v2 offset:62464
	v_mfma_f32_16x16x32_f16 v[76:79], v[72:75], v[24:27], v[76:79]
	v_exp_f32_e32 v112, v112
	v_exp_f32_e32 v113, v113
	v_exp_f32_e32 v114, v114
	v_exp_f32_e32 v115, v115
	s_waitcnt lgkmcnt(2)
	v_mfma_f32_32x32x16_f16 v[96:111], v[32:35], v[28:31], 0
	v_fmac_f32_e32 v144, v112, v143
	v_exp_f32_e32 v116, v116
	v_fmac_f32_e32 v145, v113, v144
	v_exp_f32_e32 v117, v117
	v_fmac_f32_e32 v146, v114, v145
	v_cvt_pkrtz_f16_f32 v68, v144, v145
	v_exp_f32_e32 v118, v118
	v_fmac_f32_e32 v147, v115, v146
	v_pk_mul_f16 v68, v60, v68
	v_exp_f32_e32 v119, v119
	v_mfma_f32_32x32x16_f16 v[128:143], v[36:39], v[44:47], 0
	v_fmac_f32_e32 v148, v116, v147
	v_cvt_pkrtz_f16_f32 v69, v146, v147
	v_exp_f32_e32 v120, v120
	v_fmac_f32_e32 v149, v117, v148
	v_pk_mul_f16 v69, v61, v69
	v_exp_f32_e32 v121, v121
	v_fmac_f32_e32 v150, v118, v149
	v_cvt_pkrtz_f16_f32 v70, v148, v149
	v_exp_f32_e32 v122, v122
	v_fmac_f32_e32 v151, v119, v150
	v_pk_mul_f16 v70, v62, v70
	v_exp_f32_e32 v123, v123
	v_mfma_f32_32x32x16_f16 v[128:143], v[40:43], v[48:51], v[128:143]
	v_cvt_pkrtz_f16_f32 v71, v150, v151
	v_fmac_f32_e32 v152, v120, v151
	ds_read_u16 v32, v10 offset:224
	ds_read_b128 v[36:39], v13 offset:1792
	ds_read_b128 v[40:43], v14 offset:1792
	ds_read_b128 v[44:47], v2 offset:30720
	ds_read_b128 v[48:51], v2 offset:31744
	v_pk_mul_f16 v71, v63, v71
	v_exp_f32_e32 v124, v124
	v_fmac_f32_e32 v153, v121, v152
	v_mfma_f32_16x16x32_f16 v[80:83], v[68:71], v[20:23], 0
	v_cvt_pkrtz_f16_f32 v72, v152, v153
	v_exp_f32_e32 v125, v125
	v_fmac_f32_e32 v154, v122, v153
	v_pk_mul_f16 v72, v64, v72
	v_add_f32_e32 v84, v76, v77
	v_fmac_f32_e32 v155, v123, v154
	v_cvt_pkrtz_f16_f32 v73, v154, v155
	v_exp_f32_e32 v126, v126
	v_fmac_f32_e32 v156, v124, v155
	v_pk_mul_f16 v73, v65, v73
	v_add_f32_e32 v85, v78, v79
	v_fmac_f32_e32 v157, v125, v156
	v_cvt_pkrtz_f16_f32 v74, v156, v157
	v_exp_f32_e32 v127, v127
	v_add_f32_e32 v84, v84, v85
	v_fmac_f32_e32 v158, v126, v157
	v_pk_mul_f16 v74, v66, v74
	v_fmac_f32_e32 v159, v127, v158
	v_mfma_f32_16x16x4_f32 a[16:19], v84, v15, 0
	v_cvt_pkrtz_f16_f32 v75, v158, v159
	v_pk_mul_f16 v75, v67, v75
	ds_read_b128 v[60:63], v2 offset:63488
	ds_read_b128 v[64:67], v2 offset:64512
	v_mfma_f32_16x16x32_f16 v[80:83], v[72:75], v[24:27], v[80:83]
	s_waitcnt vmcnt(0)
	ds_write_b16 v8, v18 offset:512
	ds_write_b16 v8, v19 offset:1536
	s_waitcnt lgkmcnt(0)
	s_barrier
	s_cmp_ge_u32 s40, 15
	s_cbranch_scc1 .Lscan_nodma1
	s_add_i32 m0, s32, 0x4000
	s_nop 0
	global_load_lds_dwordx4 v2, s[20:21]
	s_add_i32 m0, s32, 49152
	s_nop 0
	global_load_lds_dwordx4 v2, s[22:23]
	s_add_i32 m0, s33, 0x4000
	s_nop 0
	global_load_lds_dwordx4 v3, s[20:21]
	s_add_i32 m0, s33, 49152
	s_nop 0
	global_load_lds_dwordx4 v3, s[22:23]
	s_add_i32 m0, s34, 0x4000
	s_nop 0
	global_load_lds_dwordx4 v4, s[20:21]
	s_add_i32 m0, s34, 49152
	s_nop 0
	global_load_lds_dwordx4 v4, s[22:23]
	s_add_i32 m0, s35, 0x4000
	s_nop 0
	global_load_lds_dwordx4 v5, s[20:21]
	s_add_i32 m0, s35, 49152
	s_nop 0
	global_load_lds_dwordx4 v5, s[22:23]
	s_add_i32 m0, s28, 0x100
	s_nop 0
	global_load_lds_dword v6, s[24:25]
	global_load_ushort v18, v7, s[26:27]
	global_load_ushort v19, v7, s[26:27] offset:128
	s_add_u32 s20, s20, 0x4000
	s_addc_u32 s21, s21, 0
	s_add_u32 s22, s22, 0x4000
	s_addc_u32 s23, s23, 0
	s_add_u32 s24, s24, 0x100
	s_addc_u32 s25, s25, 0
	s_add_u32 s26, s26, 0x100
	s_addc_u32 s27, s27, 0
.Lscan_nodma1:
	s_and_saveexec_b64 s[44:45], s[42:43]
	global_store_dwordx4 v[16:17], a[20:23], off offset:-192
	global_store_dwordx4 v[16:17], a[24:27], off offset:-128
	global_store_dwordx4 v[16:17], a[28:31], off offset:-64
	global_store_dwordx4 v[16:17], a[0:3], off
	global_store_dwordx4 v[16:17], a[4:7], off offset:64
	global_store_dwordx4 v[16:17], a[8:11], off offset:128
	global_store_dwordx4 v[16:17], a[12:15], off offset:192
	global_store_dwordx4 v[16:17], a[16:19], off offset:256
	s_mov_b64 exec, s[44:45]
	v_lshl_add_u64 v[16:17], v[16:17], 0, s[46:47]
	v_exp_f32_e32 v96, v96
	v_exp_f32_e32 v97, v97
	v_exp_f32_e32 v98, v98
	v_exp_f32_e32 v99, v99
	s_waitcnt lgkmcnt(2)
	v_mfma_f32_32x32x16_f16 v[112:127], v[32:35], v[28:31], 0
	v_fmac_f32_e32 v128, v96, v159
	v_exp_f32_e32 v100, v100
	v_fmac_f32_e32 v129, v97, v128
	v_exp_f32_e32 v101, v101
	v_fmac_f32_e32 v130, v98, v129
	v_cvt_pkrtz_f16_f32 v68, v128, v129
	v_exp_f32_e32 v102, v102
	v_fmac_f32_e32 v131, v99, v130
	v_pk_mul_f16 v68, v52, v68
	v_exp_f32_e32 v103, v103
	v_mfma_f32_32x32x16_f16 v[144:159], v[36:39], v[44:47], 0
	v_fmac_f32_e32 v132, v100, v131
	v_cvt_pkrtz_f16_f32 v69, v130, v131
	v_exp_f32_e32 v104, v104
	v_fmac_f32_e32 v133, v101, v132
	v_pk_mul_f16 v69, v53, v69
	v_exp_f32_e32 v105, v105
	v_fmac_f32_e32 v134, v102, v133
	v_cvt_pkrtz_f16_f32 v70, v132, v133
	v_exp_f32_e32 v106, v106
	v_fmac_f32_e32 v135, v103, v134
	v_pk_mul_f16 v70, v54, v70
	v_exp_f32_e32 v107, v107
	v_mfma_f32_32x32x16_f16 v[144:159], v[40:43], v[48:51], v[144:159]
	v_cvt_pkrtz_f16_f32 v71, v134, v135
	v_fmac_f32_e32 v136, v104, v135
	ds_read_u16 v32, v9 offset:0
	ds_read_b128 v[36:39], v11 offset:0
	ds_read_b128 v[40:43], v12 offset:0
	ds_read_b128 v[44:47], v2 offset:0
	ds_read_b128 v[48:51], v2 offset:1024
	v_pk_mul_f16 v71, v55, v71
	v_exp_f32_e32 v108, v108
	v_fmac_f32_e32 v137, v105, v136
	v_mfma_f32_16x16x32_f16 v[76:79], v[68:71], v[20:23], 0
	v_cvt_pkrtz_f16_f32 v72, v136, v137
	v_exp_f32_e32 v109, v109
	v_fmac_f32_e32 v138, v106, v137
	v_pk_mul_f16 v72, v56, v72
	v_add_f32_e32 v84, v80, v81
	v_fmac_f32_e32 v139, v107, v138
	v_cvt_pkrtz_f16_f32 v73, v138, v139
	v_exp_f32_e32 v110, v110
	v_fmac_f32_e32 v140, v108, v139
	v_pk_mul_f16 v73, v57, v73
	v_add_f32_e32 v85, v82, v83
	v_fmac_f32_e32 v141, v109, v140
	v_cvt_pkrtz_f16_f32 v74, v140, v141
	v_exp_f32_e32 v111, v111
	v_add_f32_e32 v84, v84, v85
	v_fmac_f32_e32 v142, v110, v141
	v_pk_mul_f16 v74, v58, v74
	v_fmac_f32_e32 v143, v111, v142
	v_mfma_f32_16x16x4_f32 a[20:23], v84, v15, 0
	v_cvt_pkrtz_f16_f32 v75, v142, v143
	v_pk_mul_f16 v75, v59, v75
	ds_read_b128 v[52:55], v2 offset:32768
	ds_read_b128 v[56:59], v2 offset:33792
	v_mfma_f32_16x16x32_f16 v[76:79], v[72:75], v[24:27], v[76:79]
	v_exp_f32_e32 v112, v112
	v_exp_f32_e32 v113, v113
	v_exp_f32_e32 v114, v114
	v_exp_f32_e32 v115, v115
	s_waitcnt lgkmcnt(2)
	v_mfma_f32_32x32x16_f16 v[96:111], v[32:35], v[28:31], 0
	v_fmac_f32_e32 v144, v112, v143
	v_exp_f32_e32 v116, v116
	v_fmac_f32_e32 v145, v113, v144
	v_exp_f32_e32 v117, v117
	v_fmac_f32_e32 v146, v114, v145
	v_cvt_pkrtz_f16_f32 v68, v144, v145
	v_exp_f32_e32 v118, v118
	v_fmac_f32_e32 v147, v115, v146
	v_pk_mul_f16 v68, v60, v68
	v_exp_f32_e32 v119, v119
	v_mfma_f32_32x32x16_f16 v[128:143], v[36:39], v[44:47], 0
	v_fmac_f32_e32 v148, v116, v147
	v_cvt_pkrtz_f16_f32 v69, v146, v147
	v_exp_f32_e32 v120, v120
	v_fmac_f32_e32 v149, v117, v148
	v_pk_mul_f16 v69, v61, v69
	v_exp_f32_e32 v121, v121
	v_fmac_f32_e32 v150, v118, v149
	v_cvt_pkrtz_f16_f32 v70, v148, v149
	v_exp_f32_e32 v122, v122
	v_fmac_f32_e32 v151, v119, v150
	v_pk_mul_f16 v70, v62, v70
	v_exp_f32_e32 v123, v123
	v_mfma_f32_32x32x16_f16 v[128:143], v[40:43], v[48:51], v[128:143]
	v_cvt_pkrtz_f16_f32 v71, v150, v151
	v_fmac_f32_e32 v152, v120, v151
	ds_read_u16 v32, v9 offset:32
	ds_read_b128 v[36:39], v11 offset:256
	ds_read_b128 v[40:43], v12 offset:256
	ds_read_b128 v[44:47], v2 offset:2048
	ds_read_b128 v[48:51], v2 offset:3072
	v_pk_mul_f16 v71, v63, v71
	v_exp_f32_e32 v124, v124
	v_fmac_f32_e32 v153, v121, v152
	v_mfma_f32_16x16x32_f16 v[80:83], v[68:71], v[20:23], 0
	v_cvt_pkrtz_f16_f32 v72, v152, v153
	v_exp_f32_e32 v125, v125
	v_fmac_f32_e32 v154, v122, v153
	v_pk_mul_f16 v72, v64, v72
	v_add_f32_e32 v84, v76, v77
	v_fmac_f32_e32 v155, v123, v154
	v_cvt_pkrtz_f16_f32 v73, v154, v155
	v_exp_f32_e32 v126, v126
	v_fmac_f32_e32 v156, v124, v155
	v_pk_mul_f16 v73, v65, v73
	v_add_f32_e32 v85, v78, v79
	v_fmac_f32_e32 v157, v125, v156
	v_cvt_pkrtz_f16_f32 v74, v156, v157
	v_exp_f32_e32 v127, v127
	v_add_f32_e32 v84, v84, v85
	v_fmac_f32_e32 v158, v126, v157
	v_pk_mul_f16 v74, v66, v74
	v_fmac_f32_e32 v159, v127, v158
	v_mfma_f32_16x16x4_f32 a[24:27], v84, v15, 0
	v_cvt_pkrtz_f16_f32 v75, v158, v159
	v_pk_mul_f16 v75, v67, v75
	s_add_u32 s40, s40, 1
	s_cmp_lt_u32 s40, 16
	s_cbranch_scc1 .Lscan_loop
	s_nop 1
	v_mfma_f32_16x16x32_f16 v[80:83], v[72:75], v[24:27], v[80:83]
	s_nop 15
	v_add_f32_e32 v84, v80, v81
	v_add_f32_e32 v85, v82, v83
	s_nop 0
	v_add_f32_e32 v84, v84, v85
	s_nop 1
	v_mfma_f32_16x16x4_f32 a[28:31], v84, v15, 0
	s_nop 15
	s_nop 3
	s_and_saveexec_b64 s[44:45], s[42:43]
	global_store_dwordx4 v[16:17], a[20:23], off offset:-192
	global_store_dwordx4 v[16:17], a[24:27], off offset:-128
	global_store_dwordx4 v[16:17], a[28:31], off offset:-64
	s_endpgm

	.amdhsa_kernel _Z6scan_kPKDF16_S0_S0_S0_PKfPf
		.amdhsa_group_segment_fixed_size 86016
		.amdhsa_private_segment_fixed_size 0
		.amdhsa_kernarg_size 48
		.amdhsa_user_sgpr_count 2
		.amdhsa_user_sgpr_dispatch_ptr 0
		.amdhsa_user_sgpr_queue_ptr 0
		.amdhsa_user_sgpr_kernarg_segment_ptr 1
		.amdhsa_user_sgpr_dispatch_id 0
		.amdhsa_user_sgpr_kernarg_preload_length 0
		.amdhsa_user_sgpr_kernarg_preload_offset 0
		.amdhsa_user_sgpr_private_segment_size 0
		.amdhsa_uses_dynamic_stack 0
		.amdhsa_enable_private_segment 0
		.amdhsa_system_sgpr_workgroup_id_x 1
		.amdhsa_system_sgpr_workgroup_id_y 0
		.amdhsa_system_sgpr_workgroup_id_z 0
		.amdhsa_system_sgpr_workgroup_info 0
		.amdhsa_system_vgpr_workitem_id 0
		.amdhsa_next_free_vgpr 192
		.amdhsa_next_free_sgpr 96
		.amdhsa_accum_offset 160
		.amdhsa_reserve_vcc 1
		.amdhsa_float_round_mode_32 0
		.amdhsa_float_round_mode_16_64 0
		.amdhsa_float_denorm_mode_32 3
		.amdhsa_float_denorm_mode_16_64 3
		.amdhsa_dx10_clamp 1
		.amdhsa_ieee_mode 1
		.amdhsa_fp16_overflow 0
		.amdhsa_tg_split 0
		.amdhsa_exception_fp_ieee_invalid_op 0
		.amdhsa_exception_fp_denorm_src 0
		.amdhsa_exception_fp_ieee_div_zero 0
		.amdhsa_exception_fp_ieee_overflow 0
		.amdhsa_exception_fp_ieee_underflow 0
		.amdhsa_exception_fp_ieee_inexact 0
		.amdhsa_exception_int_div_zero 0
	.end_amdhsa_kernel

	.section	.text._Z6gemm_gILi32ELi64ELi16ELi32ELi1ELi0ELi64ELi4EEv5GemmP,"axG",@progbits,_Z6gemm_gILi32ELi64ELi16ELi32ELi1ELi0ELi64ELi4EEv5GemmP,comdat
	.p2alignl 8, 3212836864

	.section	.text._Z6gemm_gILi64ELi64ELi32ELi32ELi1ELi0ELi64ELi4EEv5GemmP,"axG",@progbits,_Z6gemm_gILi64ELi64ELi32ELi32ELi1ELi0ELi64ELi4EEv5GemmP,comdat
	.p2alignl 8, 3212836864

	.section	.text._Z6gemm_gILi64ELi128ELi32ELi64ELi0ELi2ELi64ELi3EEv5GemmP,"axG",@progbits,_Z6gemm_gILi64ELi128ELi32ELi64ELi0ELi2ELi64ELi3EEv5GemmP,comdat
	.p2alignl 8, 3212836864

	.section	.text._Z6gemm_gILi64ELi64ELi32ELi32ELi0ELi3ELi64ELi3EEv5GemmP,"axG",@progbits,_Z6gemm_gILi64ELi64ELi32ELi32ELi0ELi3ELi64ELi3EEv5GemmP,comdat
	.p2alignl 8, 3212836864

	.section	.text._Z6gemm_gILi64ELi64ELi32ELi32ELi0ELi4ELi64ELi3EEv5GemmP,"axG",@progbits,_Z6gemm_gILi64ELi64ELi32ELi32ELi0ELi4ELi64ELi3EEv5GemmP,comdat
	.p2alignl 8, 3212836864

	.section	.text._Z6gemm_gILi32ELi64ELi16ELi32ELi1ELi1ELi128ELi3EEv5GemmP,"axG",@progbits,_Z6gemm_gILi32ELi64ELi16ELi32ELi1ELi1ELi128ELi3EEv5GemmP,comdat
	.p2alignl 8, 3212836864

	.section	.text._Z6gemm_gILi32ELi64ELi16ELi32ELi1ELi1ELi64ELi4EEv5GemmP,"axG",@progbits,_Z6gemm_gILi32ELi64ELi16ELi32ELi1ELi1ELi64ELi4EEv5GemmP,comdat
	.p2alignl 8, 3212836864

	.text
	.p2alignl 8, 3212836864
	.fill 256, 4, 3212836864

amdhsa.kernels:
  - .agpr_count:     0
    .args:
      - .offset:         0
        .size:           152
        .value_kind:     by_value
    .group_segment_fixed_size: 7168
    .kernarg_segment_align: 8
    .kernarg_segment_size: 152
    .language:       OpenCL C
    .language_version:
      - 2
      - 0
    .max_flat_workgroup_size: 256
    .name:           _Z6prep_k5PrepP
    .private_segment_fixed_size: 0
    .sgpr_count:     62
    .sgpr_spill_count: 0
    .symbol:         _Z6prep_k5PrepP.kd
    .uniform_work_group_size: 1
    .uses_dynamic_stack: false
    .vgpr_count:     58
    .vgpr_spill_count: 0
    .wavefront_size: 64
  - .agpr_count:     0
    .args:
      - .actual_access:  read_only
        .address_space:  global
        .offset:         0
        .size:           8
        .value_kind:     global_buffer
      - .actual_access:  read_only
        .address_space:  global
        .offset:         8
        .size:           8
        .value_kind:     global_buffer
      - .actual_access:  read_only
        .address_space:  global
        .offset:         16
        .size:           8
        .value_kind:     global_buffer
      - .actual_access:  write_only
        .address_space:  global
        .offset:         24
        .size:           8
        .value_kind:     global_buffer
      - .actual_access:  write_only
        .address_space:  global
        .offset:         32
        .size:           8
        .value_kind:     global_buffer
    .group_segment_fixed_size: 9216
    .kernarg_segment_align: 8
    .kernarg_segment_size: 40
    .language:       OpenCL C
    .language_version:
      - 2
      - 0
    .max_flat_workgroup_size: 256
    .name:           _Z8conv1d_kPKDF16_PKfS2_PDF16_S3_
    .private_segment_fixed_size: 0
    .sgpr_count:     22
    .sgpr_spill_count: 0
    .symbol:         _Z8conv1d_kPKDF16_PKfS2_PDF16_S3_.kd
    .uniform_work_group_size: 1
    .uses_dynamic_stack: false
    .vgpr_count:     53
    .vgpr_spill_count: 0
    .wavefront_size: 64
  - .agpr_count:     4
    .args:
      - .actual_access:  read_only
        .address_space:  global
        .offset:         0
        .size:           8
        .value_kind:     global_buffer
      - .actual_access:  read_only
        .address_space:  global
        .offset:         8
        .size:           8
        .value_kind:     global_buffer
      - .actual_access:  read_only
        .address_space:  global
        .offset:         16
        .size:           8
        .value_kind:     global_buffer
      - .actual_access:  read_only
        .address_space:  global
        .offset:         24
        .size:           8
        .value_kind:     global_buffer
      - .actual_access:  write_only
        .address_space:  global
        .offset:         32
        .size:           8
        .value_kind:     global_buffer
      - .actual_access:  write_only
        .address_space:  global
        .offset:         40
        .size:           8
        .value_kind:     global_buffer
    .group_segment_fixed_size: 70656
    .kernarg_segment_align: 8
    .kernarg_segment_size: 48
    .language:       OpenCL C
    .language_version:
      - 2
      - 0
    .max_flat_workgroup_size: 256
    .name:           _Z4dt_kPKfS0_S0_PKDF16_PDF16_S3_
    .private_segment_fixed_size: 0
    .sgpr_count:     25
    .sgpr_spill_count: 0
    .symbol:         _Z4dt_kPKfS0_S0_PKDF16_PDF16_S3_.kd
    .uniform_work_group_size: 1
    .uses_dynamic_stack: false
    .vgpr_count:     72
    .vgpr_spill_count: 0
    .wavefront_size: 64
  - .agpr_count:     32
    .args:
      - .address_space:  global
        .offset:         0
        .size:           8
        .value_kind:     global_buffer
      - .actual_access:  read_only
        .address_space:  global
        .offset:         8
        .size:           8
        .value_kind:     global_buffer
      - .address_space:  global
        .offset:         16
        .size:           8
        .value_kind:     global_buffer
      - .address_space:  global
        .offset:         24
        .size:           8
        .value_kind:     global_buffer
      - .actual_access:  read_only
        .address_space:  global
        .offset:         32
        .size:           8
        .value_kind:     global_buffer
      - .actual_access:  write_only
        .address_space:  global
        .offset:         40
        .size:           8
        .value_kind:     global_buffer
    .group_segment_fixed_size: 86016
    .kernarg_segment_align: 8
    .kernarg_segment_size: 48
    .language:       OpenCL C
    .language_version:
      - 2
      - 0
    .max_flat_workgroup_size: 256
    .name:           _Z6scan_kPKDF16_S0_S0_S0_PKfPf
    .private_segment_fixed_size: 0
    .sgpr_count:     66
    .sgpr_spill_count: 0
    .symbol:         _Z6scan_kPKDF16_S0_S0_S0_PKfPf.kd
    .uniform_work_group_size: 1
    .uses_dynamic_stack: false
    .vgpr_count:     192
    .vgpr_spill_count: 0
    .wavefront_size: 64
  - .agpr_count:     0
    .args:
      - .actual_access:  read_only
        .address_space:  global
        .offset:         0
        .size:           8
        .value_kind:     global_buffer
      - .actual_access:  read_only
        .address_space:  global
        .offset:         8
        .size:           8
        .value_kind:     global_buffer
      - .actual_access:  read_only
        .address_space:  global
        .offset:         16
        .size:           8
        .value_kind:     global_buffer
      - .actual_access:  read_only
        .address_space:  global
        .offset:         24
        .size:           8
        .value_kind:     global_buffer
      - .actual_access:  write_only
        .address_space:  global
        .offset:         32
        .size:           8
        .value_kind:     global_buffer
    .group_segment_fixed_size: 9216
    .kernarg_segment_align: 8
    .kernarg_segment_size: 40
    .language:       OpenCL C
    .language_version:
      - 2
      - 0
    .max_flat_workgroup_size: 256
    .name:           _Z6gate_kPKfPKDF16_S2_S0_PDF16_
    .private_segment_fixed_size: 0
    .sgpr_count:     22
    .sgpr_spill_count: 0
    .symbol:         _Z6gate_kPKfPKDF16_S2_S0_PDF16_.kd
    .uniform_work_group_size: 1
    .uses_dynamic_stack: false
    .vgpr_count:     46
    .vgpr_spill_count: 0
    .wavefront_size: 64
  - .agpr_count:     0
    .args:
      - .actual_access:  read_only
        .address_space:  global
        .offset:         0
        .size:           8
        .value_kind:     global_buffer
      - .actual_access:  read_only
        .address_space:  global
        .offset:         8
        .size:           8
        .value_kind:     global_buffer
      - .actual_access:  read_only
        .address_space:  global
        .offset:         16
        .size:           8
        .value_kind:     global_buffer
      - .actual_access:  write_only
        .address_space:  global
        .offset:         24
        .size:           8
        .value_kind:     global_buffer
    .group_segment_fixed_size: 6912
    .kernarg_segment_align: 8
    .kernarg_segment_size: 32
    .language:       OpenCL C
    .language_version:
      - 2
      - 0
    .max_flat_workgroup_size: 256
    .name:           _Z9deconv3_kPKDF16_PKfS2_Pf
    .private_segment_fixed_size: 0
    .sgpr_count:     26
    .sgpr_spill_count: 0
    .symbol:         _Z9deconv3_kPKDF16_PKfS2_Pf.kd
    .uniform_work_group_size: 1
    .uses_dynamic_stack: false
    .vgpr_count:     55
    .vgpr_spill_count: 0
    .wavefront_size: 64
  - .agpr_count:     8
    .args:
      - .offset:         0
        .size:           112
        .value_kind:     by_value
    .group_segment_fixed_size: 49152
    .kernarg_segment_align: 8
    .kernarg_segment_size: 112
    .language:       OpenCL C
    .language_version:
      - 2
      - 0
    .max_flat_workgroup_size: 256
    .name:           _Z6gemm_gILi32ELi64ELi16ELi32ELi1ELi0ELi64ELi4EEv5GemmP
    .private_segment_fixed_size: 0
    .sgpr_count:     34
    .sgpr_spill_count: 0
    .symbol:         _Z6gemm_gILi32ELi64ELi16ELi32ELi1ELi0ELi64ELi4EEv5GemmP.kd
    .uniform_work_group_size: 1
    .uses_dynamic_stack: false
    .vgpr_count:     40
    .vgpr_spill_count: 0
    .wavefront_size: 64
  - .agpr_count:     16
    .args:
      - .offset:         0
        .size:           112
        .value_kind:     by_value
    .group_segment_fixed_size: 65536
    .kernarg_segment_align: 8
    .kernarg_segment_size: 112
    .language:       OpenCL C
    .language_version:
      - 2
      - 0
    .max_flat_workgroup_size: 256
    .name:           _Z6gemm_gILi64ELi64ELi32ELi32ELi1ELi0ELi64ELi4EEv5GemmP
    .private_segment_fixed_size: 0
    .sgpr_count:     34
    .sgpr_spill_count: 0
    .symbol:         _Z6gemm_gILi64ELi64ELi32ELi32ELi1ELi0ELi64ELi4EEv5GemmP.kd
    .uniform_work_group_size: 1
    .uses_dynamic_stack: false
    .vgpr_count:     56
    .vgpr_spill_count: 0
    .wavefront_size: 64
  - .agpr_count:     32
    .args:
      - .offset:         0
        .size:           112
        .value_kind:     by_value
    .group_segment_fixed_size: 73728
    .kernarg_segment_align: 8
    .kernarg_segment_size: 112
    .language:       OpenCL C
    .language_version:
      - 2
      - 0
    .max_flat_workgroup_size: 256
    .name:           _Z6gemm_gILi64ELi128ELi32ELi64ELi0ELi2ELi64ELi3EEv5GemmP
    .private_segment_fixed_size: 0
    .sgpr_count:     27
    .sgpr_spill_count: 0
    .symbol:         _Z6gemm_gILi64ELi128ELi32ELi64ELi0ELi2ELi64ELi3EEv5GemmP.kd
    .uniform_work_group_size: 1
    .uses_dynamic_stack: false
    .vgpr_count:     80
    .vgpr_spill_count: 0
    .wavefront_size: 64
  - .agpr_count:     16
    .args:
      - .offset:         0
        .size:           112
        .value_kind:     by_value
    .group_segment_fixed_size: 49152
    .kernarg_segment_align: 8
    .kernarg_segment_size: 112
    .language:       OpenCL C
    .language_version:
      - 2
      - 0
    .max_flat_workgroup_size: 256
    .name:           _Z6gemm_gILi64ELi64ELi32ELi32ELi0ELi3ELi64ELi3EEv5GemmP
    .private_segment_fixed_size: 0
    .sgpr_count:     30
    .sgpr_spill_count: 0
    .symbol:         _Z6gemm_gILi64ELi64ELi32ELi32ELi0ELi3ELi64ELi3EEv5GemmP.kd
    .uniform_work_group_size: 1
    .uses_dynamic_stack: false
    .vgpr_count:     56
    .vgpr_spill_count: 0
    .wavefront_size: 64
  - .agpr_count:     16
    .args:
      - .offset:         0
        .size:           112
        .value_kind:     by_value
    .group_segment_fixed_size: 49152
    .kernarg_segment_align: 8
    .kernarg_segment_size: 112
    .language:       OpenCL C
    .language_version:
      - 2
      - 0
    .max_flat_workgroup_size: 256
    .name:           _Z6gemm_gILi64ELi64ELi32ELi32ELi0ELi4ELi64ELi3EEv5GemmP
    .private_segment_fixed_size: 0
    .sgpr_count:     27
    .sgpr_spill_count: 0
    .symbol:         _Z6gemm_gILi64ELi64ELi32ELi32ELi0ELi4ELi64ELi3EEv5GemmP.kd
    .uniform_work_group_size: 1
    .uses_dynamic_stack: false
    .vgpr_count:     52
    .vgpr_spill_count: 0
    .wavefront_size: 64
  - .agpr_count:     8
    .args:
      - .offset:         0
        .size:           112
        .value_kind:     by_value
    .group_segment_fixed_size: 73728
    .kernarg_segment_align: 8
    .kernarg_segment_size: 112
    .language:       OpenCL C
    .language_version:
      - 2
      - 0
    .max_flat_workgroup_size: 256
    .name:           _Z6gemm_gILi32ELi64ELi16ELi32ELi1ELi1ELi128ELi3EEv5GemmP
    .private_segment_fixed_size: 0
    .sgpr_count:     38
    .sgpr_spill_count: 0
    .symbol:         _Z6gemm_gILi32ELi64ELi16ELi32ELi1ELi1ELi128ELi3EEv5GemmP.kd
    .uniform_work_group_size: 1
    .uses_dynamic_stack: false
    .vgpr_count:     48
    .vgpr_spill_count: 0
    .wavefront_size: 64
  - .agpr_count:     8
    .args:
      - .offset:         0
        .size:           112
        .value_kind:     by_value
    .group_segment_fixed_size: 49152
    .kernarg_segment_align: 8
    .kernarg_segment_size: 112
    .language:       OpenCL C
    .language_version:
      - 2
      - 0
    .max_flat_workgroup_size: 256
    .name:           _Z6gemm_gILi32ELi64ELi16ELi32ELi1ELi1ELi64ELi4EEv5GemmP
    .private_segment_fixed_size: 0
    .sgpr_count:     36
    .sgpr_spill_count: 0
    .symbol:         _Z6gemm_gILi32ELi64ELi16ELi32ELi1ELi1ELi64ELi4EEv5GemmP.kd
    .uniform_work_group_size: 1
    .uses_dynamic_stack: false
    .vgpr_count:     40
    .vgpr_spill_count: 0
    .wavefront_size: 64
